# v65 + conv/pool phase: silu and window-count reciprocals by v_rcp_f32 instead of the expanded IEEE division
# speedup vs baseline: 1.0261x; 1.0029x over previous
; #define LAS __attribute__((address_space(3)))
; __device__ __forceinline__ unsigned pk2(float lo, float hi) { return (unsigned)f2bf(lo) | ((unsigned)f2bf(hi) << 16); }
; __device__ __forceinline__ float sigmoidf_(float x) { return 1.0f / (1.0f + __expf(-x)); }
; __device__ __forceinline__ void ph_convpool_fast(const Args& a, LAS unsigned char* lds) {
;     ...
;             const int tl = 4 * wave + j, t = t0 + tl; const size_t tok = (size_t)tok0 + tl;
;             const int cnt = (t + 1 < wnd) ? (t + 1) : wnd;
;             float s[8], self[8];
;             unpack8(*(const LAS u32x4*)(lds + UT_OFF + (15 + tl) * 1024 + ch * 2), self);
; #pragma unroll
;             for (int c = 0; c < 8; ++c) s[c] = self[c];
;             for (int k = 1; k < cnt; ++k) { float v[8]; unpack8(*(const LAS u32x4*)(lds + UT_OFF + (15 + tl - k) * 1024 + ch * 2), v);
; #pragma unroll
;                 for (int c = 0; c < 8; ++c) s[c] += v[c]; }
;             const float inv = 1.0f / (float)cnt;
;             u32x4 o; o.x = pk2(s[0] * inv - self[0], s[1] * inv - self[1]); o.y = pk2(s[2] * inv - self[2], s[3] * inv - self[3]);
;             o.z = pk2(s[4] * inv - self[4], s[5] * inv - self[5]); o.w = pk2(s[6] * inv - self[6], s[7] * inv - self[7]);
;             *(u32x4*)(CAT + tok * 1024 + ch) = o;
;             float sm = 0.f;
; #pragma unroll
;             for (int c = 0; c < 8; ++c) sm += acc[j][c];
;             const float mean = wave_sum(sm) * (1.0f / 512.0f);
;             float sq = 0.f;
; #pragma unroll
;             for (int c = 0; c < 8; ++c) { acc[j][c] -= mean; sq += acc[j][c] * acc[j][c]; }
;             const float rstd = rsqrtf(wave_sum(sq) * (1.0f / 512.0f) + LN_EPS);
;             float y[8];
; #pragma unroll
;             for (int c = 0; c < 8; ++c) { const float z = acc[j][c] * rstd * gam[c] + bet[c]; y[c] = z * sigmoidf_(z); }
;             u32x4 o2; o2.x = pk2(y[0], y[1]); o2.y = pk2(y[2], y[3]); o2.z = pk2(y[4], y[5]); o2.w = pk2(y[6], y[7]);
;             *(u32x4*)(CAT + tok * 1024 + 512 + ch) = o2;
.LBB0_269:
	s_or_b64 exec, exec, s[2:3]
	v_add_u32_e32 v62, s20, v44
	v_min_u32_e32 v62, v62, v144
	v_cvt_f32_ubyte0_e32 v64, v62
	v_lshl_add_u64 v[62:63], s[0:1], 0, v[44:45]
	s_add_i32 s19, s19, s12
	s_add_i32 s13, s13, s14
	v_rcp_f32_e32 v64, v64
	s_nop 0
	v_pk_fma_f32 v[28:29], v[64:65], v[58:59], v[28:29] op_sel_hi:[0,1,1] neg_lo:[0,0,1] neg_hi:[0,0,1]
	v_pk_fma_f32 v[32:33], v[64:65], v[34:35], v[32:33] op_sel_hi:[0,1,1] neg_lo:[0,0,1] neg_hi:[0,0,1]
	v_pk_fma_f32 v[26:27], v[64:65], v[60:61], v[26:27] op_sel_hi:[0,1,1] neg_lo:[0,0,1] neg_hi:[0,0,1]
	v_pk_fma_f32 v[30:31], v[64:65], v[36:37], v[30:31] op_sel_hi:[0,1,1] neg_lo:[0,0,1] neg_hi:[0,0,1]
	v_bfe_u32 v34, v33, 16, 1
	v_bfe_u32 v35, v32, 16, 1
	v_bfe_u32 v36, v29, 16, 1
	v_bfe_u32 v37, v28, 16, 1
	v_add3_u32 v58, v28, v37, s17
	v_add3_u32 v59, v29, v36, s17
	v_add3_u32 v28, v32, v35, s17
	v_add3_u32 v29, v33, v34, s17
	v_bfe_u32 v32, v26, 16, 1
	v_bfe_u32 v34, v30, 16, 1
	v_add3_u32 v30, v30, v34, s17
	v_add3_u32 v26, v26, v32, s17
	v_lshrrev_b32_e32 v60, 16, v26
	v_lshrrev_b32_e32 v26, 16, v30
	v_and_or_b32 v28, v28, s16, v26
	v_add_f32_e32 v26, 0, v56
	v_add_f32_e32 v26, v54, v26
	v_add_f32_e32 v26, v57, v26
	v_add_f32_e32 v26, v55, v26
	v_add_f32_e32 v26, v16, v26
	v_add_f32_e32 v26, v12, v26
	v_add_f32_e32 v26, v17, v26
	v_add_f32_e32 v26, v13, v26
	v_bfe_u32 v33, v27, 16, 1
	v_bfe_u32 v35, v31, 16, 1
	v_add_f32_dpp v26, v26, v26 quad_perm:[1,0,3,2] row_mask:0xf bank_mask:0xf bound_ctrl:1
	v_add3_u32 v31, v31, v35, s17
	v_add3_u32 v27, v27, v33, s17
	v_add_f32_dpp v26, v26, v26 quad_perm:[2,3,0,1] row_mask:0xf bank_mask:0xf bound_ctrl:1
	v_lshrrev_b32_e32 v61, 16, v27
	v_lshrrev_b32_e32 v27, 16, v31
	v_add_f32_dpp v26, v26, v26 row_half_mirror row_mask:0xf bank_mask:0xf bound_ctrl:1
	v_and_or_b32 v29, v29, s16, v27
	s_cmpk_lt_i32 s19, 0x400
	v_add_f32_dpp v26, v26, v26 row_mirror row_mask:0xf bank_mask:0xf bound_ctrl:1
	s_nop 0
	v_readlane_b32 s2, v26, 16
	v_readlane_b32 s3, v26, 48
	v_readlane_b32 s0, v26, 0
	v_readlane_b32 s1, v26, 32
	v_mov_b32_e32 v26, s2
	v_mov_b32_e32 v27, s3
	v_pk_add_f32 v[26:27], s[0:1], v[26:27]
	s_nop 0
	v_add_f32_e32 v26, v26, v27
	v_mul_f32_e32 v26, 0x3b000000, v26
	v_pk_add_f32 v[30:31], v[56:57], v[26:27] op_sel_hi:[1,0] neg_lo:[0,1] neg_hi:[0,1]
	v_pk_add_f32 v[32:33], v[54:55], v[26:27] op_sel_hi:[1,0] neg_lo:[0,1] neg_hi:[0,1]
	v_mov_b32_e32 v35, v31
	v_mov_b32_e32 v34, v33
	v_mul_f32_e32 v54, v30, v30
	v_pk_mul_f32 v[34:35], v[34:35], v[34:35]
	v_pk_add_f32 v[16:17], v[16:17], v[26:27] op_sel_hi:[1,0] neg_lo:[0,1] neg_hi:[0,1]
	v_pk_add_f32 v[12:13], v[12:13], v[26:27] op_sel_hi:[1,0] neg_lo:[0,1] neg_hi:[0,1]
	v_fmac_f32_e32 v54, v32, v32
	v_mov_b32_e32 v26, v12
	v_mov_b32_e32 v27, v16
	v_add_f32_e32 v35, v35, v54
	v_pk_mul_f32 v[26:27], v[26:27], v[26:27]
	v_add_f32_e32 v34, v34, v35
	v_mov_b32_e32 v36, v13
	v_mov_b32_e32 v37, v17
	v_add_f32_e32 v27, v27, v34
	v_pk_mul_f32 v[36:37], v[36:37], v[36:37]
	v_add_f32_e32 v26, v26, v27
	v_add_f32_e32 v26, v37, v26
	v_add_f32_e32 v26, v36, v26
	v_lshlrev_b64 v[34:35], 11, v[62:63]
	v_lshl_add_u64 v[34:35], v[48:49], 0, v[34:35]
	v_add_f32_dpp v26, v26, v26 quad_perm:[1,0,3,2] row_mask:0xf bank_mask:0xf bound_ctrl:1
	s_nop 1
	v_add_f32_dpp v26, v26, v26 quad_perm:[2,3,0,1] row_mask:0xf bank_mask:0xf bound_ctrl:1
	s_nop 1
	v_add_f32_dpp v26, v26, v26 row_half_mirror row_mask:0xf bank_mask:0xf bound_ctrl:1
	s_nop 1
	v_add_f32_dpp v26, v26, v26 row_mirror row_mask:0xf bank_mask:0xf bound_ctrl:1
	s_nop 0
	v_readlane_b32 s2, v26, 16
	v_readlane_b32 s3, v26, 48
	v_readlane_b32 s0, v26, 0
	v_readlane_b32 s1, v26, 32
	v_mov_b32_e32 v26, s2
	v_mov_b32_e32 v27, s3
	v_pk_add_f32 v[26:27], s[0:1], v[26:27]
	s_nop 0
	v_add_f32_e32 v26, v26, v27
	v_fmamk_f32 v26, v26, 0x3b000000, v170
	v_mul_f32_e32 v27, 0x4b800000, v26
	v_cmp_gt_f32_e32 vcc, s18, v26
	s_nop 1
	v_cndmask_b32_e32 v26, v26, v27, vcc
	v_rsq_f32_e32 v36, v26
	v_and_or_b32 v27, v59, s16, v61
	v_and_or_b32 v26, v58, s16, v60
	global_store_dwordx4 v[34:35], v[26:29], off
	v_mul_f32_e32 v37, 0x45800000, v36
	v_cndmask_b32_e32 v36, v36, v37, vcc
	v_pk_mul_f32 v[30:31], v[30:31], v[36:37] op_sel_hi:[1,0]
	s_nop 0
	v_pk_fma_f32 v[30:31], v[6:7], v[30:31], v[2:3]
	s_nop 0
	v_mul_f32_e32 v37, 0xbfb8aa3b, v30
	v_exp_f32_e32 v54, v37
	v_mul_f32_e32 v37, 0xbfb8aa3b, v31
	v_exp_f32_e32 v55, v37
	v_pk_mul_f32 v[26:27], v[32:33], v[36:37] op_sel_hi:[1,0]
	v_pk_add_f32 v[28:29], v[54:55], 1.0 op_sel_hi:[1,0]
	s_nop 0
	v_pk_fma_f32 v[26:27], v[52:53], v[26:27], v[50:51]
	v_rcp_f32_e32 v29, v29
	v_mul_f32_e32 v32, 0xbfb8aa3b, v26
	v_mul_f32_e32 v33, 0xbfb8aa3b, v27
	v_exp_f32_e32 v32, v32
	v_exp_f32_e32 v33, v33
	s_nop 0
	v_pk_add_f32 v[32:33], v[32:33], 1.0 op_sel_hi:[1,0]
	v_rcp_f32_e32 v28, v28
	s_nop 0
	v_pk_mul_f32 v[28:29], v[30:31], v[28:29]
	v_rcp_f32_e32 v31, v33
	v_pk_mul_f32 v[16:17], v[16:17], v[36:37] op_sel_hi:[1,0]
	v_pk_fma_f32 v[16:17], v[14:15], v[16:17], v[10:11]
	v_mul_f32_e32 v33, 0xbfb8aa3b, v16
	v_exp_f32_e32 v54, v33
	v_mul_f32_e32 v33, 0xbfb8aa3b, v17
	v_exp_f32_e32 v55, v33
	v_rcp_f32_e32 v30, v32
	s_nop 0
	v_pk_mul_f32 v[26:27], v[26:27], v[30:31]
	v_pk_mul_f32 v[12:13], v[12:13], v[36:37] op_sel_hi:[1,0]
	v_pk_add_f32 v[30:31], v[54:55], 1.0 op_sel_hi:[1,0]
	v_pk_fma_f32 v[12:13], v[8:9], v[12:13], v[4:5]
	v_mul_f32_e32 v32, 0xbfb8aa3b, v12
	v_exp_f32_e32 v32, v32
	v_rcp_f32_e32 v31, v31
	v_mul_f32_e32 v33, 0xbfb8aa3b, v13
	v_exp_f32_e32 v33, v33
	s_nop 0
	v_pk_add_f32 v[32:33], v[32:33], 1.0 op_sel_hi:[1,0]
	v_rcp_f32_e32 v30, v30
	s_nop 0
	v_pk_mul_f32 v[16:17], v[16:17], v[30:31]
	v_rcp_f32_e32 v31, v33
	v_rcp_f32_e32 v30, v32
	s_nop 0
	v_pk_mul_f32 v[12:13], v[12:13], v[30:31]
	v_bfe_u32 v32, v27, 16, 1
	v_bfe_u32 v30, v13, 16, 1
	v_bfe_u32 v31, v12, 16, 1
	v_bfe_u32 v33, v26, 16, 1
	v_add3_u32 v26, v26, v33, s17
	v_add3_u32 v27, v27, v32, s17
	v_add3_u32 v12, v12, v31, s17
	v_add3_u32 v13, v13, v30, s17
	v_bfe_u32 v30, v28, 16, 1
	v_bfe_u32 v31, v29, 16, 1
	v_bfe_u32 v32, v16, 16, 1
	v_bfe_u32 v33, v17, 16, 1
	v_add3_u32 v17, v17, v33, s17
	v_add3_u32 v16, v16, v32, s17
	v_add3_u32 v29, v29, v31, s17
	v_add3_u32 v28, v28, v30, s17
	v_lshrrev_b32_e32 v30, 16, v28
	v_lshrrev_b32_e32 v31, 16, v29
	v_lshrrev_b32_e32 v16, 16, v16
	v_lshrrev_b32_e32 v17, 16, v17
	v_and_or_b32 v29, v13, s16, v17
	v_and_or_b32 v28, v12, s16, v16
	v_and_or_b32 v27, v27, s16, v31
	v_and_or_b32 v26, v26, s16, v30
	global_store_dwordx4 v[34:35], v[26:29], off offset:1024
	s_cbranch_scc0 .LBB0_337

; #define LAS __attribute__((address_space(3)))
; __device__ __forceinline__ unsigned pk2(float lo, float hi) { return (unsigned)f2bf(lo) | ((unsigned)f2bf(hi) << 16); }
; __device__ __forceinline__ float sigmoidf_(float x) { return 1.0f / (1.0f + __expf(-x)); }
; __device__ __forceinline__ void ph_convpool_fast(const Args& a, LAS unsigned char* lds) {
;     ...
;             const int tl = 4 * wave + j, t = t0 + tl; const size_t tok = (size_t)tok0 + tl;
;             const int cnt = (t + 1 < wnd) ? (t + 1) : wnd;
;             float s[8], self[8];
;             unpack8(*(const LAS u32x4*)(lds + UT_OFF + (15 + tl) * 1024 + ch * 2), self);
; #pragma unroll
;             for (int c = 0; c < 8; ++c) s[c] = self[c];
;             for (int k = 1; k < cnt; ++k) { float v[8]; unpack8(*(const LAS u32x4*)(lds + UT_OFF + (15 + tl - k) * 1024 + ch * 2), v);
; #pragma unroll
;                 for (int c = 0; c < 8; ++c) s[c] += v[c]; }
;             const float inv = 1.0f / (float)cnt;
;             u32x4 o; o.x = pk2(s[0] * inv - self[0], s[1] * inv - self[1]); o.y = pk2(s[2] * inv - self[2], s[3] * inv - self[3]);
;             o.z = pk2(s[4] * inv - self[4], s[5] * inv - self[5]); o.w = pk2(s[6] * inv - self[6], s[7] * inv - self[7]);
;             *(u32x4*)(CAT + tok * 1024 + ch) = o;
;             float sm = 0.f;
; #pragma unroll
;             for (int c = 0; c < 8; ++c) sm += acc[j][c];
;             const float mean = wave_sum(sm) * (1.0f / 512.0f);
;             float sq = 0.f;
; #pragma unroll
;             for (int c = 0; c < 8; ++c) { acc[j][c] -= mean; sq += acc[j][c] * acc[j][c]; }
;             const float rstd = rsqrtf(wave_sum(sq) * (1.0f / 512.0f) + LN_EPS);
;             float y[8];
; #pragma unroll
;             for (int c = 0; c < 8; ++c) { const float z = acc[j][c] * rstd * gam[c] + bet[c]; y[c] = z * sigmoidf_(z); }
;             u32x4 o2; o2.x = pk2(y[0], y[1]); o2.y = pk2(y[2], y[3]); o2.z = pk2(y[4], y[5]); o2.w = pk2(y[6], y[7]);
;             *(u32x4*)(CAT + tok * 1024 + 512 + ch) = o2;
.LBB0_313:
	s_or_b64 exec, exec, s[2:3]
	v_min_u32_e32 v86, v86, v144
	v_cvt_f32_ubyte0_e32 v88, v86
	s_ashr_i32 s1, s0, 31
	v_lshl_add_u64 v[86:87], s[0:1], 0, v[38:39]
	v_add_u32_e32 v94, -2, v178
	v_rcp_f32_e32 v88, v88
	v_mov_b32_e32 v90, v83
	v_mov_b32_e32 v92, v29
	v_mov_b32_e32 v83, v84
	v_mov_b32_e32 v29, v32
	v_mov_b32_e32 v91, v85
	v_mov_b32_e32 v93, v33
	v_pk_fma_f32 v[28:29], v[88:89], v[82:83], v[28:29] op_sel_hi:[0,1,1] neg_lo:[0,0,1] neg_hi:[0,0,1]
	v_mov_b32_e32 v32, v35
	v_mov_b32_e32 v33, v37
	v_mov_b32_e32 v82, v27
	v_mov_b32_e32 v83, v31
	v_pk_fma_f32 v[90:91], v[88:89], v[90:91], v[92:93] op_sel_hi:[0,1,1] neg_lo:[0,0,1] neg_hi:[0,0,1]
	v_pk_fma_f32 v[32:33], v[88:89], v[32:33], v[82:83] op_sel_hi:[0,1,1] neg_lo:[0,0,1] neg_hi:[0,0,1]
	v_mov_b32_e32 v35, v36
	v_mov_b32_e32 v27, v30
	v_pk_fma_f32 v[26:27], v[88:89], v[34:35], v[26:27] op_sel_hi:[0,1,1] neg_lo:[0,0,1] neg_hi:[0,0,1]
	v_bfe_u32 v31, v91, 16, 1
	v_bfe_u32 v35, v33, 16, 1
	v_bfe_u32 v30, v90, 16, 1
	v_bfe_u32 v34, v32, 16, 1
	v_add3_u32 v33, v33, v35, s17
	v_add3_u32 v31, v91, v31, s17
	v_add3_u32 v32, v32, v34, s17
	v_add3_u32 v30, v90, v30, s17
	v_lshrrev_b32_e32 v83, 16, v31
	v_lshrrev_b32_e32 v31, 16, v33
	v_bfe_u32 v33, v26, 16, 1
	v_lshrrev_b32_e32 v82, 16, v30
	v_lshrrev_b32_e32 v30, 16, v32
	v_bfe_u32 v35, v28, 16, 1
	v_add3_u32 v26, v26, v33, s17
	v_add3_u32 v84, v28, v35, s17
	v_and_or_b32 v28, v26, s16, v30
	v_add_f32_e32 v26, 0, v80
	v_add_f32_e32 v26, v78, v26
	v_add_f32_e32 v26, v81, v26
	v_add_f32_e32 v26, v79, v26
	v_add_f32_e32 v26, v76, v26
	v_add_f32_e32 v26, v74, v26
	v_add_f32_e32 v26, v77, v26
	v_add_f32_e32 v26, v75, v26
	v_bfe_u32 v32, v27, 16, 1
	v_bfe_u32 v34, v29, 16, 1
	v_add_f32_dpp v26, v26, v26 quad_perm:[1,0,3,2] row_mask:0xf bank_mask:0xf bound_ctrl:1
	v_add3_u32 v27, v27, v32, s17
	v_add3_u32 v85, v29, v34, s17
	v_add_f32_dpp v26, v26, v26 quad_perm:[2,3,0,1] row_mask:0xf bank_mask:0xf bound_ctrl:1
	v_and_or_b32 v29, v27, s16, v31
	s_nop 0
	v_add_f32_dpp v26, v26, v26 row_half_mirror row_mask:0xf bank_mask:0xf bound_ctrl:1
	s_nop 1
	v_add_f32_dpp v26, v26, v26 row_mirror row_mask:0xf bank_mask:0xf bound_ctrl:1
	s_nop 0
	v_readlane_b32 s8, v26, 16
	v_readlane_b32 s9, v26, 48
	v_readlane_b32 s2, v26, 0
	v_readlane_b32 s3, v26, 32
	v_mov_b32_e32 v26, s8
	v_mov_b32_e32 v27, s9
	v_pk_add_f32 v[26:27], s[2:3], v[26:27]
	s_nop 0
	v_add_f32_e32 v26, v26, v27
	v_mul_f32_e32 v26, 0x3b000000, v26
	v_pk_add_f32 v[30:31], v[80:81], v[26:27] op_sel_hi:[1,0] neg_lo:[0,1] neg_hi:[0,1]
	v_pk_add_f32 v[32:33], v[78:79], v[26:27] op_sel_hi:[1,0] neg_lo:[0,1] neg_hi:[0,1]
	v_mov_b32_e32 v35, v31
	v_mov_b32_e32 v34, v33
	v_mul_f32_e32 v78, v30, v30
	v_pk_mul_f32 v[34:35], v[34:35], v[34:35]
	v_pk_add_f32 v[36:37], v[76:77], v[26:27] op_sel_hi:[1,0] neg_lo:[0,1] neg_hi:[0,1]
	v_pk_add_f32 v[74:75], v[74:75], v[26:27] op_sel_hi:[1,0] neg_lo:[0,1] neg_hi:[0,1]
	v_fmac_f32_e32 v78, v32, v32
	v_mov_b32_e32 v26, v74
	v_mov_b32_e32 v27, v36
	v_add_f32_e32 v35, v35, v78
	v_pk_mul_f32 v[26:27], v[26:27], v[26:27]
	v_add_f32_e32 v34, v34, v35
	v_mov_b32_e32 v76, v75
	v_mov_b32_e32 v77, v37
	v_add_f32_e32 v27, v27, v34
	v_pk_mul_f32 v[76:77], v[76:77], v[76:77]
	v_add_f32_e32 v26, v26, v27
	v_add_f32_e32 v26, v77, v26
	v_add_f32_e32 v26, v76, v26
	v_lshlrev_b64 v[34:35], 11, v[86:87]
	v_lshl_add_u64 v[34:35], v[48:49], 0, v[34:35]
	v_add_f32_dpp v26, v26, v26 quad_perm:[1,0,3,2] row_mask:0xf bank_mask:0xf bound_ctrl:1
	s_nop 1
	v_add_f32_dpp v26, v26, v26 quad_perm:[2,3,0,1] row_mask:0xf bank_mask:0xf bound_ctrl:1
	s_nop 1
	v_add_f32_dpp v26, v26, v26 row_half_mirror row_mask:0xf bank_mask:0xf bound_ctrl:1
	s_nop 1
	v_add_f32_dpp v26, v26, v26 row_mirror row_mask:0xf bank_mask:0xf bound_ctrl:1
	s_nop 0
	v_readlane_b32 s8, v26, 16
	v_readlane_b32 s9, v26, 48
	v_readlane_b32 s2, v26, 0
	v_readlane_b32 s3, v26, 32
	v_mov_b32_e32 v26, s8
	v_mov_b32_e32 v27, s9
	v_pk_add_f32 v[26:27], s[2:3], v[26:27]
	s_nop 0
	v_add_f32_e32 v26, v26, v27
	v_fmamk_f32 v26, v26, 0x3b000000, v170
	v_mul_f32_e32 v27, 0x4b800000, v26
	v_cmp_gt_f32_e32 vcc, s18, v26
	s_nop 1
	v_cndmask_b32_e32 v26, v26, v27, vcc
	v_rsq_f32_e32 v76, v26
	v_and_or_b32 v27, v85, s16, v83
	v_and_or_b32 v26, v84, s16, v82
	global_store_dwordx4 v[34:35], v[26:29], off
	v_mul_f32_e32 v77, 0x45800000, v76
	v_cndmask_b32_e32 v76, v76, v77, vcc
	v_pk_mul_f32 v[30:31], v[30:31], v[76:77] op_sel_hi:[1,0]
	s_nop 0
	v_pk_fma_f32 v[30:31], v[6:7], v[30:31], v[2:3]
	s_nop 0
	v_mul_f32_e32 v77, 0xbfb8aa3b, v30
	v_exp_f32_e32 v78, v77
	v_mul_f32_e32 v77, 0xbfb8aa3b, v31
	v_exp_f32_e32 v79, v77
	v_pk_mul_f32 v[26:27], v[32:33], v[76:77] op_sel_hi:[1,0]
	v_pk_add_f32 v[28:29], v[78:79], 1.0 op_sel_hi:[1,0]
	s_nop 0
	v_pk_fma_f32 v[26:27], v[52:53], v[26:27], v[50:51]
	v_rcp_f32_e32 v29, v29
	v_mul_f32_e32 v32, 0xbfb8aa3b, v26
	v_mul_f32_e32 v33, 0xbfb8aa3b, v27
	v_exp_f32_e32 v32, v32
	v_exp_f32_e32 v33, v33
	s_nop 0
	v_pk_add_f32 v[32:33], v[32:33], 1.0 op_sel_hi:[1,0]
	v_rcp_f32_e32 v28, v28
	s_nop 0
	v_pk_mul_f32 v[28:29], v[30:31], v[28:29]
	v_rcp_f32_e32 v31, v33
	v_pk_mul_f32 v[36:37], v[36:37], v[76:77] op_sel_hi:[1,0]
	v_pk_fma_f32 v[36:37], v[14:15], v[36:37], v[10:11]
	v_mul_f32_e32 v33, 0xbfb8aa3b, v36
	v_exp_f32_e32 v78, v33
	v_mul_f32_e32 v33, 0xbfb8aa3b, v37
	v_exp_f32_e32 v79, v33
	v_rcp_f32_e32 v30, v32
	s_nop 0
	v_pk_mul_f32 v[26:27], v[26:27], v[30:31]
	v_pk_mul_f32 v[30:31], v[74:75], v[76:77] op_sel_hi:[1,0]
	v_pk_add_f32 v[32:33], v[78:79], 1.0 op_sel_hi:[1,0]
	v_pk_fma_f32 v[30:31], v[8:9], v[30:31], v[4:5]
	v_mul_f32_e32 v74, 0xbfb8aa3b, v30
	v_exp_f32_e32 v74, v74
	v_rcp_f32_e32 v33, v33
	v_mul_f32_e32 v75, 0xbfb8aa3b, v31
	v_exp_f32_e32 v75, v75
	s_nop 0
	v_pk_add_f32 v[74:75], v[74:75], 1.0 op_sel_hi:[1,0]
	v_rcp_f32_e32 v32, v32
	s_nop 0
	v_pk_mul_f32 v[32:33], v[36:37], v[32:33]
	v_rcp_f32_e32 v37, v75
	v_mov_b32_e32 v80, 1
	v_rcp_f32_e32 v36, v74
	s_nop 0
	v_pk_mul_f32 v[30:31], v[30:31], v[36:37]
	v_bfe_u32 v75, v26, 16, 1
	v_bfe_u32 v36, v31, 16, 1
	v_bfe_u32 v37, v30, 16, 1
	v_bfe_u32 v74, v27, 16, 1
	v_add3_u32 v26, v26, v75, s17
	v_add3_u32 v37, v30, v37, s17
	v_add3_u32 v30, v31, v36, s17
	v_bfe_u32 v36, v29, 16, 1
	v_bfe_u32 v75, v33, 16, 1
	v_add3_u32 v27, v27, v74, s17
	v_bfe_u32 v31, v28, 16, 1
	v_bfe_u32 v74, v32, 16, 1
	v_add3_u32 v33, v33, v75, s17
	v_add3_u32 v29, v29, v36, s17
	v_add3_u32 v32, v32, v74, s17
	v_add3_u32 v28, v28, v31, s17
	v_lshrrev_b32_e32 v74, 16, v29
	v_lshrrev_b32_e32 v29, 16, v33
	v_lshrrev_b32_e32 v36, 16, v28
	v_lshrrev_b32_e32 v28, 16, v32
	v_and_or_b32 v29, v30, s16, v29
	ds_read_b128 v[30:33], v171 offset:63488
	v_and_or_b32 v28, v37, s16, v28
	v_and_or_b32 v27, v27, s16, v74
	v_and_or_b32 v26, v26, s16, v36
	global_store_dwordx4 v[34:35], v[26:29], off offset:1024
	v_cmp_lt_u32_e32 vcc, 6, v94
	s_waitcnt lgkmcnt(0)
; #define LAS __attribute__((address_space(3)))
; __device__ __forceinline__ void ph_convpool_fast(const Args& a, LAS unsigned char* lds) {
;     ...
;             unpack8(*(const LAS u32x4*)(lds + UT_OFF + (15 + tl) * 1024 + ch * 2), self);
; #pragma unroll
;             for (int c = 0; c < 8; ++c) s[c] = self[c];
;             for (int k = 1; k < cnt; ++k) { float v[8]; unpack8(*(const LAS u32x4*)(lds + UT_OFF + (15 + tl - k) * 1024 + ch * 2), v);
	v_lshlrev_b32_e32 v27, 16, v31
	v_lshlrev_b32_e32 v26, 16, v30
	v_and_b32_e32 v29, 0xffff0000, v31
	v_and_b32_e32 v28, 0xffff0000, v30
	v_lshlrev_b32_e32 v31, 16, v33
	v_lshlrev_b32_e32 v30, 16, v32
	v_and_b32_e32 v33, 0xffff0000, v33
	v_and_b32_e32 v32, 0xffff0000, v32
	v_mov_b64_e32 v[36:37], v[30:31]
	v_mov_b64_e32 v[34:35], v[32:33]
	v_mov_b64_e32 v[76:77], v[26:27]
	v_mov_b64_e32 v[74:75], v[28:29]
	s_and_saveexec_b64 s[2:3], vcc
	s_cbranch_execz .LBB0_317
	v_add_u32_e32 v34, -1, v177
	v_and_b32_e32 v78, -8, v34
	s_mov_b32 s10, 0
	s_mov_b64 s[8:9], 0
	v_mov_b32_e32 v79, v156
	v_mov_b64_e32 v[74:75], v[28:29]
	v_mov_b64_e32 v[76:77], v[26:27]
	v_mov_b64_e32 v[34:35], v[32:33]
	v_mov_b64_e32 v[36:37], v[30:31]

; #define LAS __attribute__((address_space(3)))
; __device__ __forceinline__ unsigned pk2(float lo, float hi) { return (unsigned)f2bf(lo) | ((unsigned)f2bf(hi) << 16); }
; __device__ __forceinline__ float sigmoidf_(float x) { return 1.0f / (1.0f + __expf(-x)); }
; __device__ __forceinline__ void ph_convpool_fast(const Args& a, LAS unsigned char* lds) {
;     ...
;             const int tl = 4 * wave + j, t = t0 + tl; const size_t tok = (size_t)tok0 + tl;
;             const int cnt = (t + 1 < wnd) ? (t + 1) : wnd;
;             float s[8], self[8];
;             unpack8(*(const LAS u32x4*)(lds + UT_OFF + (15 + tl) * 1024 + ch * 2), self);
; #pragma unroll
;             for (int c = 0; c < 8; ++c) s[c] = self[c];
;             for (int k = 1; k < cnt; ++k) { float v[8]; unpack8(*(const LAS u32x4*)(lds + UT_OFF + (15 + tl - k) * 1024 + ch * 2), v);
; #pragma unroll
;                 for (int c = 0; c < 8; ++c) s[c] += v[c]; }
;             const float inv = 1.0f / (float)cnt;
;             u32x4 o; o.x = pk2(s[0] * inv - self[0], s[1] * inv - self[1]); o.y = pk2(s[2] * inv - self[2], s[3] * inv - self[3]);
;             o.z = pk2(s[4] * inv - self[4], s[5] * inv - self[5]); o.w = pk2(s[6] * inv - self[6], s[7] * inv - self[7]);
;             *(u32x4*)(CAT + tok * 1024 + ch) = o;
;             float sm = 0.f;
; #pragma unroll
;             for (int c = 0; c < 8; ++c) sm += acc[j][c];
;             const float mean = wave_sum(sm) * (1.0f / 512.0f);
;             float sq = 0.f;
; #pragma unroll
;             for (int c = 0; c < 8; ++c) { acc[j][c] -= mean; sq += acc[j][c] * acc[j][c]; }
;             const float rstd = rsqrtf(wave_sum(sq) * (1.0f / 512.0f) + LN_EPS);
;             float y[8];
; #pragma unroll
;             for (int c = 0; c < 8; ++c) { const float z = acc[j][c] * rstd * gam[c] + bet[c]; y[c] = z * sigmoidf_(z); }
;             u32x4 o2; o2.x = pk2(y[0], y[1]); o2.y = pk2(y[2], y[3]); o2.z = pk2(y[4], y[5]); o2.w = pk2(y[6], y[7]);
;             *(u32x4*)(CAT + tok * 1024 + 512 + ch) = o2;
.LBB0_321:
	s_or_b64 exec, exec, s[2:3]
	v_add_u32_e32 v78, s20, v40
	v_min_u32_e32 v78, v78, v144
	v_cvt_f32_ubyte0_e32 v80, v78
	v_lshl_add_u64 v[78:79], s[0:1], 0, v[40:41]
	v_add_u32_e32 v83, -2, v176
	v_rcp_f32_e32 v80, v80
	s_nop 0
	v_pk_fma_f32 v[28:29], v[80:81], v[74:75], v[28:29] op_sel_hi:[0,1,1] neg_lo:[0,0,1] neg_hi:[0,0,1]
	v_pk_fma_f32 v[32:33], v[80:81], v[34:35], v[32:33] op_sel_hi:[0,1,1] neg_lo:[0,0,1] neg_hi:[0,0,1]
	v_pk_fma_f32 v[26:27], v[80:81], v[76:77], v[26:27] op_sel_hi:[0,1,1] neg_lo:[0,0,1] neg_hi:[0,0,1]
	v_pk_fma_f32 v[30:31], v[80:81], v[36:37], v[30:31] op_sel_hi:[0,1,1] neg_lo:[0,0,1] neg_hi:[0,0,1]
	v_bfe_u32 v34, v33, 16, 1
	v_bfe_u32 v35, v32, 16, 1
	v_bfe_u32 v36, v29, 16, 1
	v_bfe_u32 v37, v28, 16, 1
	v_add3_u32 v74, v28, v37, s17
	v_add3_u32 v75, v29, v36, s17
	v_add3_u32 v28, v32, v35, s17
	v_add3_u32 v29, v33, v34, s17
	v_bfe_u32 v32, v26, 16, 1
	v_bfe_u32 v34, v30, 16, 1
	v_add3_u32 v30, v30, v34, s17
	v_add3_u32 v26, v26, v32, s17
	v_lshrrev_b32_e32 v76, 16, v26
	v_lshrrev_b32_e32 v26, 16, v30
	v_and_or_b32 v28, v28, s16, v26
	v_add_f32_e32 v26, 0, v72
	v_add_f32_e32 v26, v70, v26
	v_add_f32_e32 v26, v73, v26
	v_add_f32_e32 v26, v71, v26
	v_add_f32_e32 v26, v68, v26
	v_add_f32_e32 v26, v66, v26
	v_add_f32_e32 v26, v69, v26
	v_add_f32_e32 v26, v67, v26
	v_bfe_u32 v33, v27, 16, 1
	v_bfe_u32 v35, v31, 16, 1
	v_add_f32_dpp v26, v26, v26 quad_perm:[1,0,3,2] row_mask:0xf bank_mask:0xf bound_ctrl:1
	v_add3_u32 v31, v31, v35, s17
	v_add3_u32 v27, v27, v33, s17
	v_add_f32_dpp v26, v26, v26 quad_perm:[2,3,0,1] row_mask:0xf bank_mask:0xf bound_ctrl:1
	v_lshrrev_b32_e32 v77, 16, v27
	v_lshrrev_b32_e32 v27, 16, v31
	v_add_f32_dpp v26, v26, v26 row_half_mirror row_mask:0xf bank_mask:0xf bound_ctrl:1
	v_and_or_b32 v29, v29, s16, v27
	s_nop 0
	v_add_f32_dpp v26, v26, v26 row_mirror row_mask:0xf bank_mask:0xf bound_ctrl:1
	s_nop 0
	v_readlane_b32 s8, v26, 16
	v_readlane_b32 s9, v26, 48
	v_readlane_b32 s2, v26, 0
	v_readlane_b32 s3, v26, 32
	v_mov_b32_e32 v26, s8
	v_mov_b32_e32 v27, s9
	v_pk_add_f32 v[26:27], s[2:3], v[26:27]
	s_nop 0
	v_add_f32_e32 v26, v26, v27
	v_mul_f32_e32 v26, 0x3b000000, v26
	v_pk_add_f32 v[30:31], v[72:73], v[26:27] op_sel_hi:[1,0] neg_lo:[0,1] neg_hi:[0,1]
	v_pk_add_f32 v[32:33], v[70:71], v[26:27] op_sel_hi:[1,0] neg_lo:[0,1] neg_hi:[0,1]
	v_mov_b32_e32 v35, v31
	v_mov_b32_e32 v34, v33
	v_mul_f32_e32 v70, v30, v30
	v_pk_mul_f32 v[34:35], v[34:35], v[34:35]
	v_pk_add_f32 v[36:37], v[68:69], v[26:27] op_sel_hi:[1,0] neg_lo:[0,1] neg_hi:[0,1]
	v_pk_add_f32 v[66:67], v[66:67], v[26:27] op_sel_hi:[1,0] neg_lo:[0,1] neg_hi:[0,1]
	v_fmac_f32_e32 v70, v32, v32
	v_mov_b32_e32 v26, v66
	v_mov_b32_e32 v27, v36
	v_add_f32_e32 v35, v35, v70
	v_pk_mul_f32 v[26:27], v[26:27], v[26:27]
	v_add_f32_e32 v34, v34, v35
	v_mov_b32_e32 v68, v67
	v_mov_b32_e32 v69, v37
	v_add_f32_e32 v27, v27, v34
	v_pk_mul_f32 v[68:69], v[68:69], v[68:69]
	v_add_f32_e32 v26, v26, v27
	v_add_f32_e32 v26, v69, v26
	v_add_f32_e32 v26, v68, v26
	v_lshlrev_b64 v[34:35], 11, v[78:79]
	v_lshl_add_u64 v[34:35], v[48:49], 0, v[34:35]
	v_add_f32_dpp v26, v26, v26 quad_perm:[1,0,3,2] row_mask:0xf bank_mask:0xf bound_ctrl:1
	s_nop 1
	v_add_f32_dpp v26, v26, v26 quad_perm:[2,3,0,1] row_mask:0xf bank_mask:0xf bound_ctrl:1
	s_nop 1
	v_add_f32_dpp v26, v26, v26 row_half_mirror row_mask:0xf bank_mask:0xf bound_ctrl:1
	s_nop 1
	v_add_f32_dpp v26, v26, v26 row_mirror row_mask:0xf bank_mask:0xf bound_ctrl:1
	s_nop 0
	v_readlane_b32 s8, v26, 16
	v_readlane_b32 s9, v26, 48
	v_readlane_b32 s2, v26, 0
	v_readlane_b32 s3, v26, 32
	v_mov_b32_e32 v26, s8
	v_mov_b32_e32 v27, s9
	v_pk_add_f32 v[26:27], s[2:3], v[26:27]
	s_nop 0
	v_add_f32_e32 v26, v26, v27
	v_fmamk_f32 v26, v26, 0x3b000000, v170
	v_mul_f32_e32 v27, 0x4b800000, v26
	v_cmp_gt_f32_e32 vcc, s18, v26
	s_nop 1
	v_cndmask_b32_e32 v26, v26, v27, vcc
	v_rsq_f32_e32 v68, v26
	v_and_or_b32 v27, v75, s16, v77
	v_and_or_b32 v26, v74, s16, v76
	global_store_dwordx4 v[34:35], v[26:29], off
	v_mul_f32_e32 v69, 0x45800000, v68
	v_cndmask_b32_e32 v68, v68, v69, vcc
	v_pk_mul_f32 v[30:31], v[30:31], v[68:69] op_sel_hi:[1,0]
	s_nop 0
	v_pk_fma_f32 v[30:31], v[6:7], v[30:31], v[2:3]
	s_nop 0
	v_mul_f32_e32 v69, 0xbfb8aa3b, v30
	v_exp_f32_e32 v70, v69
	v_mul_f32_e32 v69, 0xbfb8aa3b, v31
	v_exp_f32_e32 v71, v69
	v_pk_mul_f32 v[26:27], v[32:33], v[68:69] op_sel_hi:[1,0]
	v_pk_add_f32 v[28:29], v[70:71], 1.0 op_sel_hi:[1,0]
	s_nop 0
	v_pk_fma_f32 v[26:27], v[52:53], v[26:27], v[50:51]
	v_rcp_f32_e32 v29, v29
	v_mul_f32_e32 v32, 0xbfb8aa3b, v26
	v_mul_f32_e32 v33, 0xbfb8aa3b, v27
	v_exp_f32_e32 v32, v32
	v_exp_f32_e32 v33, v33
	s_nop 0
	v_pk_add_f32 v[32:33], v[32:33], 1.0 op_sel_hi:[1,0]
	v_rcp_f32_e32 v28, v28
	s_nop 0
	v_pk_mul_f32 v[28:29], v[30:31], v[28:29]
	v_rcp_f32_e32 v31, v33
	v_pk_mul_f32 v[36:37], v[36:37], v[68:69] op_sel_hi:[1,0]
	v_pk_fma_f32 v[36:37], v[14:15], v[36:37], v[10:11]
	v_mul_f32_e32 v33, 0xbfb8aa3b, v36
	v_exp_f32_e32 v70, v33
	v_mul_f32_e32 v33, 0xbfb8aa3b, v37
	v_exp_f32_e32 v71, v33
	v_rcp_f32_e32 v30, v32
	s_nop 0
	v_pk_mul_f32 v[26:27], v[26:27], v[30:31]
	v_pk_mul_f32 v[30:31], v[66:67], v[68:69] op_sel_hi:[1,0]
	v_pk_add_f32 v[32:33], v[70:71], 1.0 op_sel_hi:[1,0]
	v_pk_fma_f32 v[30:31], v[8:9], v[30:31], v[4:5]
	v_mul_f32_e32 v66, 0xbfb8aa3b, v30
	v_exp_f32_e32 v66, v66
	v_rcp_f32_e32 v33, v33
	v_mul_f32_e32 v67, 0xbfb8aa3b, v31
	v_exp_f32_e32 v67, v67
	s_nop 0
	v_pk_add_f32 v[66:67], v[66:67], 1.0 op_sel_hi:[1,0]
	v_rcp_f32_e32 v32, v32
	s_nop 0
	v_pk_mul_f32 v[32:33], v[36:37], v[32:33]
	v_rcp_f32_e32 v37, v67
	v_mov_b32_e32 v72, 1
	v_rcp_f32_e32 v36, v66
	s_nop 0
	v_pk_mul_f32 v[30:31], v[30:31], v[36:37]
	v_bfe_u32 v67, v26, 16, 1
	v_bfe_u32 v36, v31, 16, 1
	v_bfe_u32 v37, v30, 16, 1
	v_bfe_u32 v66, v27, 16, 1
	v_add3_u32 v26, v26, v67, s17
	v_add3_u32 v37, v30, v37, s17
	v_add3_u32 v30, v31, v36, s17
	v_bfe_u32 v36, v29, 16, 1
	v_bfe_u32 v67, v33, 16, 1
	v_add3_u32 v27, v27, v66, s17
	v_bfe_u32 v31, v28, 16, 1
	v_bfe_u32 v66, v32, 16, 1
	v_add3_u32 v33, v33, v67, s17
	v_add3_u32 v29, v29, v36, s17
	v_add3_u32 v32, v32, v66, s17
	v_add3_u32 v28, v28, v31, s17
	v_lshrrev_b32_e32 v66, 16, v29
	v_lshrrev_b32_e32 v29, 16, v33
	v_lshrrev_b32_e32 v36, 16, v28
	v_lshrrev_b32_e32 v28, 16, v32
	v_and_or_b32 v29, v30, s16, v29
	ds_read_b128 v[30:33], v172 offset:63488
	v_and_or_b32 v28, v37, s16, v28
	v_and_or_b32 v27, v27, s16, v66
	v_and_or_b32 v26, v26, s16, v36
	global_store_dwordx4 v[34:35], v[26:29], off offset:1024
	v_cmp_lt_u32_e32 vcc, 6, v83
	s_waitcnt lgkmcnt(0)
	v_lshlrev_b32_e32 v27, 16, v31
	v_lshlrev_b32_e32 v26, 16, v30
	v_and_b32_e32 v29, 0xffff0000, v31
	v_and_b32_e32 v28, 0xffff0000, v30
	v_lshlrev_b32_e32 v31, 16, v33
	v_lshlrev_b32_e32 v30, 16, v32
	v_and_b32_e32 v33, 0xffff0000, v33
	v_and_b32_e32 v32, 0xffff0000, v32
	v_mov_b64_e32 v[36:37], v[30:31]
	v_mov_b64_e32 v[34:35], v[32:33]
	v_mov_b64_e32 v[68:69], v[26:27]
	v_mov_b64_e32 v[66:67], v[28:29]
	s_and_saveexec_b64 s[2:3], vcc
	s_cbranch_execz .LBB0_325
; #define LAS __attribute__((address_space(3)))
; __device__ __forceinline__ void ph_convpool_fast(const Args& a, LAS unsigned char* lds) {
;     ...
;             for (int c = 0; c < 8; ++c) s[c] = self[c];
;             for (int k = 1; k < cnt; ++k) { float v[8]; unpack8(*(const LAS u32x4*)(lds + UT_OFF + (15 + tl - k) * 1024 + ch * 2), v);
	v_add_u32_e32 v34, -1, v175
	v_and_b32_e32 v70, -8, v34
	s_mov_b32 s10, 0
	s_mov_b64 s[8:9], 0
	v_mov_b32_e32 v71, v158
	v_mov_b64_e32 v[66:67], v[28:29]
	v_mov_b64_e32 v[68:69], v[26:27]
	v_mov_b64_e32 v[34:35], v[32:33]
	v_mov_b64_e32 v[36:37], v[30:31]

; #define LAS __attribute__((address_space(3)))
; __device__ __forceinline__ unsigned pk2(float lo, float hi) { return (unsigned)f2bf(lo) | ((unsigned)f2bf(hi) << 16); }
; __device__ __forceinline__ float sigmoidf_(float x) { return 1.0f / (1.0f + __expf(-x)); }
; __device__ __forceinline__ void ph_convpool_fast(const Args& a, LAS unsigned char* lds) {
;     ...
;             const int tl = 4 * wave + j, t = t0 + tl; const size_t tok = (size_t)tok0 + tl;
;             const int cnt = (t + 1 < wnd) ? (t + 1) : wnd;
;             float s[8], self[8];
;             unpack8(*(const LAS u32x4*)(lds + UT_OFF + (15 + tl) * 1024 + ch * 2), self);
; #pragma unroll
;             for (int c = 0; c < 8; ++c) s[c] = self[c];
;             for (int k = 1; k < cnt; ++k) { float v[8]; unpack8(*(const LAS u32x4*)(lds + UT_OFF + (15 + tl - k) * 1024 + ch * 2), v);
; #pragma unroll
;                 for (int c = 0; c < 8; ++c) s[c] += v[c]; }
;             const float inv = 1.0f / (float)cnt;
;             u32x4 o; o.x = pk2(s[0] * inv - self[0], s[1] * inv - self[1]); o.y = pk2(s[2] * inv - self[2], s[3] * inv - self[3]);
;             o.z = pk2(s[4] * inv - self[4], s[5] * inv - self[5]); o.w = pk2(s[6] * inv - self[6], s[7] * inv - self[7]);
;             *(u32x4*)(CAT + tok * 1024 + ch) = o;
;             float sm = 0.f;
; #pragma unroll
;             for (int c = 0; c < 8; ++c) sm += acc[j][c];
;             const float mean = wave_sum(sm) * (1.0f / 512.0f);
;             float sq = 0.f;
; #pragma unroll
;             for (int c = 0; c < 8; ++c) { acc[j][c] -= mean; sq += acc[j][c] * acc[j][c]; }
;             const float rstd = rsqrtf(wave_sum(sq) * (1.0f / 512.0f) + LN_EPS);
;             float y[8];
; #pragma unroll
;             for (int c = 0; c < 8; ++c) { const float z = acc[j][c] * rstd * gam[c] + bet[c]; y[c] = z * sigmoidf_(z); }
;             u32x4 o2; o2.x = pk2(y[0], y[1]); o2.y = pk2(y[2], y[3]); o2.z = pk2(y[4], y[5]); o2.w = pk2(y[6], y[7]);
;             *(u32x4*)(CAT + tok * 1024 + 512 + ch) = o2;
.LBB0_329:
	s_or_b64 exec, exec, s[2:3]
	v_add_u32_e32 v70, s20, v42
	v_min_u32_e32 v70, v70, v144
	v_cvt_f32_ubyte0_e32 v72, v70
	v_lshl_add_u64 v[70:71], s[0:1], 0, v[42:43]
	v_add_u32_e32 v75, -2, v174
	v_rcp_f32_e32 v72, v72
	s_nop 0
	v_pk_fma_f32 v[28:29], v[72:73], v[66:67], v[28:29] op_sel_hi:[0,1,1] neg_lo:[0,0,1] neg_hi:[0,0,1]
	v_pk_fma_f32 v[32:33], v[72:73], v[34:35], v[32:33] op_sel_hi:[0,1,1] neg_lo:[0,0,1] neg_hi:[0,0,1]
	v_pk_fma_f32 v[26:27], v[72:73], v[68:69], v[26:27] op_sel_hi:[0,1,1] neg_lo:[0,0,1] neg_hi:[0,0,1]
	v_pk_fma_f32 v[30:31], v[72:73], v[36:37], v[30:31] op_sel_hi:[0,1,1] neg_lo:[0,0,1] neg_hi:[0,0,1]
	v_bfe_u32 v34, v33, 16, 1
	v_bfe_u32 v35, v32, 16, 1
	v_bfe_u32 v36, v29, 16, 1
	v_bfe_u32 v37, v28, 16, 1
	v_add3_u32 v66, v28, v37, s17
	v_add3_u32 v67, v29, v36, s17
	v_add3_u32 v28, v32, v35, s17
	v_add3_u32 v29, v33, v34, s17
	v_bfe_u32 v32, v26, 16, 1
	v_bfe_u32 v34, v30, 16, 1
	v_add3_u32 v30, v30, v34, s17
	v_add3_u32 v26, v26, v32, s17
	v_lshrrev_b32_e32 v68, 16, v26
	v_lshrrev_b32_e32 v26, 16, v30
	v_and_or_b32 v28, v28, s16, v26
	v_add_f32_e32 v26, 0, v64
	v_add_f32_e32 v26, v62, v26
	v_add_f32_e32 v26, v65, v26
	v_add_f32_e32 v26, v63, v26
	v_add_f32_e32 v26, v60, v26
	v_add_f32_e32 v26, v58, v26
	v_add_f32_e32 v26, v61, v26
	v_add_f32_e32 v26, v59, v26
	v_bfe_u32 v33, v27, 16, 1
	v_bfe_u32 v35, v31, 16, 1
	v_add_f32_dpp v26, v26, v26 quad_perm:[1,0,3,2] row_mask:0xf bank_mask:0xf bound_ctrl:1
	v_add3_u32 v31, v31, v35, s17
	v_add3_u32 v27, v27, v33, s17
	v_add_f32_dpp v26, v26, v26 quad_perm:[2,3,0,1] row_mask:0xf bank_mask:0xf bound_ctrl:1
	v_lshrrev_b32_e32 v69, 16, v27
	v_lshrrev_b32_e32 v27, 16, v31
	v_add_f32_dpp v26, v26, v26 row_half_mirror row_mask:0xf bank_mask:0xf bound_ctrl:1
	v_and_or_b32 v29, v29, s16, v27
	s_nop 0
	v_add_f32_dpp v26, v26, v26 row_mirror row_mask:0xf bank_mask:0xf bound_ctrl:1
	s_nop 0
	v_readlane_b32 s8, v26, 16
	v_readlane_b32 s9, v26, 48
	v_readlane_b32 s2, v26, 0
	v_readlane_b32 s3, v26, 32
	v_mov_b32_e32 v26, s8
	v_mov_b32_e32 v27, s9
	v_pk_add_f32 v[26:27], s[2:3], v[26:27]
	s_nop 0
	v_add_f32_e32 v26, v26, v27
	v_mul_f32_e32 v26, 0x3b000000, v26
	v_pk_add_f32 v[30:31], v[64:65], v[26:27] op_sel_hi:[1,0] neg_lo:[0,1] neg_hi:[0,1]
	v_pk_add_f32 v[32:33], v[62:63], v[26:27] op_sel_hi:[1,0] neg_lo:[0,1] neg_hi:[0,1]
	v_mov_b32_e32 v35, v31
	v_mov_b32_e32 v34, v33
	v_mul_f32_e32 v62, v30, v30
	v_pk_mul_f32 v[34:35], v[34:35], v[34:35]
	v_pk_add_f32 v[36:37], v[60:61], v[26:27] op_sel_hi:[1,0] neg_lo:[0,1] neg_hi:[0,1]
	v_pk_add_f32 v[58:59], v[58:59], v[26:27] op_sel_hi:[1,0] neg_lo:[0,1] neg_hi:[0,1]
	v_fmac_f32_e32 v62, v32, v32
	v_mov_b32_e32 v26, v58
	v_mov_b32_e32 v27, v36
	v_add_f32_e32 v35, v35, v62
	v_pk_mul_f32 v[26:27], v[26:27], v[26:27]
	v_add_f32_e32 v34, v34, v35
	v_mov_b32_e32 v60, v59
	v_mov_b32_e32 v61, v37
	v_add_f32_e32 v27, v27, v34
	v_pk_mul_f32 v[60:61], v[60:61], v[60:61]
	v_add_f32_e32 v26, v26, v27
	v_add_f32_e32 v26, v61, v26
	v_add_f32_e32 v26, v60, v26
	v_lshlrev_b64 v[34:35], 11, v[70:71]
	v_lshl_add_u64 v[34:35], v[48:49], 0, v[34:35]
	v_add_f32_dpp v26, v26, v26 quad_perm:[1,0,3,2] row_mask:0xf bank_mask:0xf bound_ctrl:1
	s_nop 1
	v_add_f32_dpp v26, v26, v26 quad_perm:[2,3,0,1] row_mask:0xf bank_mask:0xf bound_ctrl:1
	s_nop 1
	v_add_f32_dpp v26, v26, v26 row_half_mirror row_mask:0xf bank_mask:0xf bound_ctrl:1
	s_nop 1
	v_add_f32_dpp v26, v26, v26 row_mirror row_mask:0xf bank_mask:0xf bound_ctrl:1
	s_nop 0
	v_readlane_b32 s8, v26, 16
	v_readlane_b32 s9, v26, 48
	v_readlane_b32 s2, v26, 0
	v_readlane_b32 s3, v26, 32
	v_mov_b32_e32 v26, s8
	v_mov_b32_e32 v27, s9
	v_pk_add_f32 v[26:27], s[2:3], v[26:27]
	s_nop 0
	v_add_f32_e32 v26, v26, v27
	v_fmamk_f32 v26, v26, 0x3b000000, v170
	v_mul_f32_e32 v27, 0x4b800000, v26
	v_cmp_gt_f32_e32 vcc, s18, v26
	s_nop 1
	v_cndmask_b32_e32 v26, v26, v27, vcc
	v_rsq_f32_e32 v60, v26
	v_and_or_b32 v27, v67, s16, v69
	v_and_or_b32 v26, v66, s16, v68
	global_store_dwordx4 v[34:35], v[26:29], off
	v_mul_f32_e32 v61, 0x45800000, v60
	v_cndmask_b32_e32 v60, v60, v61, vcc
	v_pk_mul_f32 v[30:31], v[30:31], v[60:61] op_sel_hi:[1,0]
	s_nop 0
	v_pk_fma_f32 v[30:31], v[6:7], v[30:31], v[2:3]
	s_nop 0
	v_mul_f32_e32 v61, 0xbfb8aa3b, v30
	v_exp_f32_e32 v62, v61
	v_mul_f32_e32 v61, 0xbfb8aa3b, v31
	v_exp_f32_e32 v63, v61
	v_pk_mul_f32 v[26:27], v[32:33], v[60:61] op_sel_hi:[1,0]
	v_pk_add_f32 v[28:29], v[62:63], 1.0 op_sel_hi:[1,0]
	s_nop 0
	v_pk_fma_f32 v[26:27], v[52:53], v[26:27], v[50:51]
	v_rcp_f32_e32 v29, v29
	v_mul_f32_e32 v32, 0xbfb8aa3b, v26
	v_mul_f32_e32 v33, 0xbfb8aa3b, v27
	v_exp_f32_e32 v32, v32
	v_exp_f32_e32 v33, v33
	s_nop 0
	v_pk_add_f32 v[32:33], v[32:33], 1.0 op_sel_hi:[1,0]
	v_rcp_f32_e32 v28, v28
	s_nop 0
	v_pk_mul_f32 v[28:29], v[30:31], v[28:29]
	v_rcp_f32_e32 v31, v33
	v_pk_mul_f32 v[36:37], v[36:37], v[60:61] op_sel_hi:[1,0]
	v_pk_fma_f32 v[36:37], v[14:15], v[36:37], v[10:11]
	v_mul_f32_e32 v33, 0xbfb8aa3b, v36
	v_exp_f32_e32 v62, v33
	v_mul_f32_e32 v33, 0xbfb8aa3b, v37
	v_exp_f32_e32 v63, v33
	v_rcp_f32_e32 v30, v32
	s_nop 0
	v_pk_mul_f32 v[26:27], v[26:27], v[30:31]
	v_pk_mul_f32 v[30:31], v[58:59], v[60:61] op_sel_hi:[1,0]
	v_pk_add_f32 v[32:33], v[62:63], 1.0 op_sel_hi:[1,0]
	v_pk_fma_f32 v[30:31], v[8:9], v[30:31], v[4:5]
	v_mul_f32_e32 v58, 0xbfb8aa3b, v30
	v_exp_f32_e32 v58, v58
	v_mov_b32_e32 v65, 1
	v_rcp_f32_e32 v33, v33
	v_mul_f32_e32 v59, 0xbfb8aa3b, v31
	v_exp_f32_e32 v59, v59
	s_nop 0
	v_pk_add_f32 v[58:59], v[58:59], 1.0 op_sel_hi:[1,0]
	v_rcp_f32_e32 v32, v32
	s_nop 0
	v_pk_mul_f32 v[32:33], v[36:37], v[32:33]
	v_rcp_f32_e32 v37, v59
	v_rcp_f32_e32 v36, v58
	s_nop 0
	v_pk_mul_f32 v[30:31], v[30:31], v[36:37]
	v_bfe_u32 v59, v26, 16, 1
	v_bfe_u32 v36, v31, 16, 1
	v_bfe_u32 v37, v30, 16, 1
	v_bfe_u32 v58, v27, 16, 1
	v_add3_u32 v26, v26, v59, s17
	v_add3_u32 v37, v30, v37, s17
	v_add3_u32 v30, v31, v36, s17
	v_bfe_u32 v36, v29, 16, 1
	v_bfe_u32 v59, v33, 16, 1
	v_add3_u32 v27, v27, v58, s17
	v_bfe_u32 v31, v28, 16, 1
	v_bfe_u32 v58, v32, 16, 1
	v_add3_u32 v33, v33, v59, s17
	v_add3_u32 v29, v29, v36, s17
	v_add3_u32 v32, v32, v58, s17
	v_add3_u32 v28, v28, v31, s17
	v_lshrrev_b32_e32 v58, 16, v29
	v_lshrrev_b32_e32 v29, 16, v33
	v_lshrrev_b32_e32 v36, 16, v28
	v_lshrrev_b32_e32 v28, 16, v32
	v_and_or_b32 v29, v30, s16, v29
	ds_read_b128 v[30:33], v173 offset:63488
	v_and_or_b32 v28, v37, s16, v28
	v_and_or_b32 v27, v27, s16, v58
	v_and_or_b32 v26, v26, s16, v36
	global_store_dwordx4 v[34:35], v[26:29], off offset:1024
	v_cmp_lt_u32_e32 vcc, 6, v75
	v_add_u32_e32 v62, -1, v174
	s_waitcnt lgkmcnt(0)
	v_lshlrev_b32_e32 v27, 16, v31
	v_lshlrev_b32_e32 v26, 16, v30
	v_and_b32_e32 v29, 0xffff0000, v31
	v_and_b32_e32 v28, 0xffff0000, v30
	v_lshlrev_b32_e32 v31, 16, v33
	v_lshlrev_b32_e32 v30, 16, v32
	v_and_b32_e32 v33, 0xffff0000, v33
	v_and_b32_e32 v32, 0xffff0000, v32
	v_mov_b64_e32 v[36:37], v[30:31]
	v_mov_b64_e32 v[34:35], v[32:33]
	v_mov_b64_e32 v[60:61], v[26:27]
	v_mov_b64_e32 v[58:59], v[28:29]
	s_and_saveexec_b64 s[2:3], vcc
	s_cbranch_execz .LBB0_333
; #define LAS __attribute__((address_space(3)))
; __device__ __forceinline__ void ph_convpool_fast(const Args& a, LAS unsigned char* lds) {
;     ...
;             for (int c = 0; c < 8; ++c) s[c] = self[c];
;             for (int k = 1; k < cnt; ++k) { float v[8]; unpack8(*(const LAS u32x4*)(lds + UT_OFF + (15 + tl - k) * 1024 + ch * 2), v);
	v_and_b32_e32 v63, -8, v62
	s_mov_b32 s10, 0
	s_mov_b64 s[8:9], 0
	v_mov_b32_e32 v64, v160
	v_mov_b64_e32 v[58:59], v[28:29]
	v_mov_b64_e32 v[60:61], v[26:27]
	v_mov_b64_e32 v[34:35], v[32:33]
	v_mov_b64_e32 v[36:37], v[30:31]
